# baseline (speedup 1.0000x reference)
_Z7gemm128ILi1ELi96EEv8GemmArgs:
	s_cmp_ge_u32 s2, 0x100
	s_cbranch_scc1 .Lou_exit
	s_load_dwordx4 s[4:7], s[0:1], 0x0
	s_load_dwordx2 s[8:9], s[0:1], 0x20
	s_load_dwordx2 s[10:11], s[0:1], 0x38
	s_load_dwordx2 s[24:25], s[0:1], 0x28
	s_load_dwordx2 s[26:27], s[0:1], 0x40
	s_load_dwordx2 s[28:29], s[0:1], 0x48
	s_and_b32 s12, s2, 7
	s_lshr_b32 s13, s2, 3
	s_lshl_b32 s12, s12, 5
	s_add_u32 s12, s12, s13
	s_and_b32 s13, s12, 3
	s_lshl_b32 s30, s13, 2
	s_lshr_b32 s12, s12, 2
	s_lshl_b32 s12, s12, 7
	s_mul_i32 s13, s13, 0xc0
	v_lshrrev_b32_e32 v1, 6, v0
	v_and_b32_e32 v14, 7, v0
	v_bfe_u32 v15, v0, 4, 3
	v_xor_b32_e32 v14, v14, v15
	v_readfirstlane_b32 s14, v1
	v_lshrrev_b32_e32 v15, 3, v0
	v_mul_u32_u24_e32 v15, 0x600, v15
	v_lshl_add_u32 v2, v14, 4, v15
	s_mov_b32 s22, 0xc000
	v_add_u32_e32 v3, s22, v2
	v_add_u32_e32 v4, s22, v3
	v_add_u32_e32 v5, s22, v4
	v_add_u32_e32 v6, s22, v5
	v_add_u32_e32 v7, s22, v6
	v_and_b32_e32 v14, 15, v0
	v_bfe_u32 v15, v0, 4, 2
	v_lshrrev_b32_e32 v16, 1, v14
	v_xor_b32_e32 v16, v16, v15
	v_lshlrev_b32_e32 v16, 4, v16
	v_bfe_u32 v17, v0, 7, 1
	v_bfe_u32 v18, v0, 6, 1
	v_lshl_add_u32 v19, v17, 6, v14
	v_lshl_add_u32 v8, v19, 7, v16
	v_mul_u32_u24_e32 v19, 0x60, v18
	v_add_u32_e32 v19, v19, v14
	v_lshl_add_u32 v9, v19, 7, v16
	v_add_u32_e32 v9, 0x4000, v9
	v_lshl_add_u32 v19, v17, 6, v14
	v_add_u32_e32 v19, s12, v19
	v_mul_u32_u24_e32 v19, 0xc00, v19
	v_mul_u32_u24_e32 v60, 0x60, v18
	v_lshl_add_u32 v60, v15, 2, v60
	v_add_u32_e32 v60, s13, v60
	v_lshl_add_u32 v56, v60, 2, v19
	s_mov_b32 s22, 0xc000
	v_add_u32_e32 v57, s22, v56
	v_add_u32_e32 v58, s22, v57
	v_add_u32_e32 v59, s22, v58
	s_waitcnt lgkmcnt(0)
	s_mul_i32 s22, s12, 0x600
	s_add_u32 s16, s4, s22
	s_addc_u32 s17, s5, 0
	s_mul_i32 s22, s13, 0x600
	s_add_u32 s18, s6, s22
	s_addc_u32 s19, s7, 0
	s_lshl_b32 s20, s14, 10
	s_mov_b32 s21, 0
	s_add_u32 m0, s20, 0x0
	s_nop 0
	global_load_lds_dwordx4 v2, s[16:17]
	s_add_u32 m0, s20, 0x1000
	s_nop 0
	global_load_lds_dwordx4 v3, s[16:17]
	s_add_u32 m0, s20, 0x2000
	s_nop 0
	global_load_lds_dwordx4 v4, s[16:17]
	s_add_u32 m0, s20, 0x3000
	s_nop 0
	global_load_lds_dwordx4 v5, s[16:17]
	s_add_u32 m0, s20, 0x4000
	s_nop 0
	global_load_lds_dwordx4 v2, s[18:19]
	s_add_u32 m0, s20, 0x5000
	s_nop 0
	global_load_lds_dwordx4 v3, s[18:19]
	s_add_u32 m0, s20, 0x6000
	s_nop 0
	global_load_lds_dwordx4 v4, s[18:19]
	s_add_u32 m0, s20, 0x7000
	s_nop 0
	global_load_lds_dwordx4 v5, s[18:19]
	s_add_u32 m0, s20, 0x8000
	s_nop 0
	global_load_lds_dwordx4 v6, s[18:19]
	s_add_u32 m0, s20, 0x9000
	s_nop 0
	global_load_lds_dwordx4 v7, s[18:19]
	s_add_u32 s16, s16, 0x80
	s_addc_u32 s17, s17, 0
	s_add_u32 s18, s18, 0x80
	s_addc_u32 s19, s19, 0
	s_add_u32 s20, s20, 0xa000
	s_sub_u32 s22, s20, 0x1e000
	s_cmp_ge_u32 s20, 0x1e000
	s_cselect_b32 s20, s22, s20
	s_add_u32 m0, s20, 0x0
	s_nop 0
	global_load_lds_dwordx4 v2, s[16:17]
	s_add_u32 m0, s20, 0x1000
	s_nop 0
	global_load_lds_dwordx4 v3, s[16:17]
	s_add_u32 m0, s20, 0x2000
	s_nop 0
	global_load_lds_dwordx4 v4, s[16:17]
	s_add_u32 m0, s20, 0x3000
	s_nop 0
	global_load_lds_dwordx4 v5, s[16:17]
	s_add_u32 m0, s20, 0x4000
	s_nop 0
	global_load_lds_dwordx4 v2, s[18:19]
	s_add_u32 m0, s20, 0x5000
	s_nop 0
	global_load_lds_dwordx4 v3, s[18:19]
	s_add_u32 m0, s20, 0x6000
	s_nop 0
	global_load_lds_dwordx4 v4, s[18:19]
	s_add_u32 m0, s20, 0x7000
	s_nop 0
	global_load_lds_dwordx4 v5, s[18:19]
	s_add_u32 m0, s20, 0x8000
	s_nop 0
	global_load_lds_dwordx4 v6, s[18:19]
	s_add_u32 m0, s20, 0x9000
	s_nop 0
	global_load_lds_dwordx4 v7, s[18:19]
	s_add_u32 s16, s16, 0x80
	s_addc_u32 s17, s17, 0
	s_add_u32 s18, s18, 0x80
	s_addc_u32 s19, s19, 0
	s_add_u32 s20, s20, 0xa000
	s_sub_u32 s22, s20, 0x1e000
	s_cmp_ge_u32 s20, 0x1e000
	s_cselect_b32 s20, s22, s20
	s_add_u32 m0, s20, 0x0
	s_nop 0
	global_load_lds_dwordx4 v2, s[16:17]
	s_add_u32 m0, s20, 0x1000
	s_nop 0
	global_load_lds_dwordx4 v3, s[16:17]
	s_add_u32 m0, s20, 0x2000
	s_nop 0
	global_load_lds_dwordx4 v4, s[16:17]
	s_add_u32 m0, s20, 0x3000
	s_nop 0
	global_load_lds_dwordx4 v5, s[16:17]
	s_add_u32 m0, s20, 0x4000
	s_nop 0
	global_load_lds_dwordx4 v2, s[18:19]
	v_mov_b32_e32 v64, 0
	v_mov_b32_e32 v65, 0
	v_mov_b32_e32 v66, 0
	v_mov_b32_e32 v67, 0
	v_mov_b32_e32 v68, 0
	v_mov_b32_e32 v69, 0
	v_mov_b32_e32 v70, 0
	v_mov_b32_e32 v71, 0
	v_mov_b32_e32 v72, 0
	v_mov_b32_e32 v73, 0
	v_mov_b32_e32 v74, 0
	v_mov_b32_e32 v75, 0
	v_mov_b32_e32 v76, 0
	v_mov_b32_e32 v77, 0
	v_mov_b32_e32 v78, 0
	v_mov_b32_e32 v79, 0
	v_mov_b32_e32 v80, 0
	v_mov_b32_e32 v81, 0
	v_mov_b32_e32 v82, 0
	v_mov_b32_e32 v83, 0
	v_mov_b32_e32 v84, 0
	v_mov_b32_e32 v85, 0
	v_mov_b32_e32 v86, 0
	v_mov_b32_e32 v87, 0
	v_mov_b32_e32 v88, 0
	v_mov_b32_e32 v89, 0
	v_mov_b32_e32 v90, 0
	v_mov_b32_e32 v91, 0
	v_mov_b32_e32 v92, 0
	v_mov_b32_e32 v93, 0
	v_mov_b32_e32 v94, 0
	v_mov_b32_e32 v95, 0
	v_mov_b32_e32 v96, 0
	v_mov_b32_e32 v97, 0
	v_mov_b32_e32 v98, 0
	v_mov_b32_e32 v99, 0
	v_mov_b32_e32 v100, 0
	v_mov_b32_e32 v101, 0
	v_mov_b32_e32 v102, 0
	v_mov_b32_e32 v103, 0
	v_mov_b32_e32 v104, 0
	v_mov_b32_e32 v105, 0
	v_mov_b32_e32 v106, 0
	v_mov_b32_e32 v107, 0
	v_mov_b32_e32 v108, 0
	v_mov_b32_e32 v109, 0
	v_mov_b32_e32 v110, 0
	v_mov_b32_e32 v111, 0
	v_mov_b32_e32 v112, 0
	v_mov_b32_e32 v113, 0
	v_mov_b32_e32 v114, 0
	v_mov_b32_e32 v115, 0
	v_mov_b32_e32 v116, 0
	v_mov_b32_e32 v117, 0
	v_mov_b32_e32 v118, 0
	v_mov_b32_e32 v119, 0
	v_mov_b32_e32 v120, 0
	v_mov_b32_e32 v121, 0
	v_mov_b32_e32 v122, 0
	v_mov_b32_e32 v123, 0
	v_mov_b32_e32 v124, 0
	v_mov_b32_e32 v125, 0
	v_mov_b32_e32 v126, 0
	v_mov_b32_e32 v127, 0
	v_mov_b32_e32 v128, 0
	v_mov_b32_e32 v129, 0
	v_mov_b32_e32 v130, 0
	v_mov_b32_e32 v131, 0
	v_mov_b32_e32 v132, 0
	v_mov_b32_e32 v133, 0
	v_mov_b32_e32 v134, 0
	v_mov_b32_e32 v135, 0
	v_mov_b32_e32 v136, 0
	v_mov_b32_e32 v137, 0
	v_mov_b32_e32 v138, 0
	v_mov_b32_e32 v139, 0
	v_mov_b32_e32 v140, 0
	v_mov_b32_e32 v141, 0
	v_mov_b32_e32 v142, 0
	v_mov_b32_e32 v143, 0
	v_mov_b32_e32 v144, 0
	v_mov_b32_e32 v145, 0
	v_mov_b32_e32 v146, 0
	v_mov_b32_e32 v147, 0
	v_mov_b32_e32 v148, 0
	v_mov_b32_e32 v149, 0
	v_mov_b32_e32 v150, 0
	v_mov_b32_e32 v151, 0
	v_mov_b32_e32 v152, 0
	v_mov_b32_e32 v153, 0
	v_mov_b32_e32 v154, 0
	v_mov_b32_e32 v155, 0
	v_mov_b32_e32 v156, 0
	v_mov_b32_e32 v157, 0
	v_mov_b32_e32 v158, 0
	v_mov_b32_e32 v159, 0
	s_waitcnt vmcnt(15)
	s_barrier
	v_add_u32_e32 v10, s21, v8
	v_add_u32_e32 v12, s21, v9
	v_xor_b32_e32 v11, 64, v10
	v_xor_b32_e32 v13, 64, v12
	s_add_u32 s21, s21, 0xa000
	s_sub_u32 s23, s21, 0x1e000
	s_cmp_ge_u32 s21, 0x1e000
	s_cselect_b32 s21, s23, s21
	ds_read_b128 v[160:163], v10 offset:0
	ds_read_b128 v[164:167], v10 offset:2048
	ds_read_b128 v[168:171], v10 offset:4096
	ds_read_b128 v[172:175], v10 offset:6144
	ds_read_b128 v[176:179], v12 offset:0
	ds_read_b128 v[180:183], v12 offset:2048
	ds_read_b128 v[184:187], v12 offset:4096
	ds_read_b128 v[188:191], v12 offset:6144
	ds_read_b128 v[192:195], v12 offset:8192
	ds_read_b128 v[196:199], v12 offset:10240
	s_mov_b32 s15, 0
.Lou_loop:
	s_waitcnt lgkmcnt(0)
	v_mfma_f32_16x16x32_bf16 v[64:67], v[176:179], v[160:163], v[64:67]
	ds_read_b128 v[200:203], v11 offset:0
	v_mfma_f32_16x16x32_bf16 v[68:71], v[176:179], v[164:167], v[68:71]
	s_add_u32 m0, s20, 0x5000
	v_mfma_f32_16x16x32_bf16 v[72:75], v[176:179], v[168:171], v[72:75]
	ds_read_b128 v[204:207], v11 offset:2048
	v_mfma_f32_16x16x32_bf16 v[76:79], v[176:179], v[172:175], v[76:79]
	global_load_lds_dwordx4 v3, s[18:19]
	v_mfma_f32_16x16x32_bf16 v[80:83], v[180:183], v[160:163], v[80:83]
	ds_read_b128 v[208:211], v11 offset:4096
	v_mfma_f32_16x16x32_bf16 v[84:87], v[180:183], v[164:167], v[84:87]
	s_add_u32 m0, s20, 0x6000
	v_mfma_f32_16x16x32_bf16 v[88:91], v[180:183], v[168:171], v[88:91]
	ds_read_b128 v[212:215], v11 offset:6144
	v_mfma_f32_16x16x32_bf16 v[92:95], v[180:183], v[172:175], v[92:95]
	global_load_lds_dwordx4 v4, s[18:19]
	v_mfma_f32_16x16x32_bf16 v[96:99], v[184:187], v[160:163], v[96:99]
	ds_read_b128 v[216:219], v13 offset:0
	v_mfma_f32_16x16x32_bf16 v[100:103], v[184:187], v[164:167], v[100:103]
	s_add_u32 m0, s20, 0x7000
	v_mfma_f32_16x16x32_bf16 v[104:107], v[184:187], v[168:171], v[104:107]
	ds_read_b128 v[220:223], v13 offset:2048
	v_mfma_f32_16x16x32_bf16 v[108:111], v[184:187], v[172:175], v[108:111]
	global_load_lds_dwordx4 v5, s[18:19]
	v_mfma_f32_16x16x32_bf16 v[112:115], v[188:191], v[160:163], v[112:115]
	ds_read_b128 v[224:227], v13 offset:4096
	v_mfma_f32_16x16x32_bf16 v[116:119], v[188:191], v[164:167], v[116:119]
	s_add_u32 m0, s20, 0x8000
	v_mfma_f32_16x16x32_bf16 v[120:123], v[188:191], v[168:171], v[120:123]
	ds_read_b128 v[228:231], v13 offset:6144
	v_mfma_f32_16x16x32_bf16 v[124:127], v[188:191], v[172:175], v[124:127]
	global_load_lds_dwordx4 v6, s[18:19]
	v_mfma_f32_16x16x32_bf16 v[128:131], v[192:195], v[160:163], v[128:131]
	ds_read_b128 v[232:235], v13 offset:8192
	v_mfma_f32_16x16x32_bf16 v[132:135], v[192:195], v[164:167], v[132:135]
	s_add_u32 m0, s20, 0x9000
	v_mfma_f32_16x16x32_bf16 v[136:139], v[192:195], v[168:171], v[136:139]
	ds_read_b128 v[236:239], v13 offset:10240
	v_mfma_f32_16x16x32_bf16 v[140:143], v[192:195], v[172:175], v[140:143]
	global_load_lds_dwordx4 v7, s[18:19]
	v_mfma_f32_16x16x32_bf16 v[144:147], v[196:199], v[160:163], v[144:147]
	s_add_u32 s16, s16, 0x80
	s_addc_u32 s17, s17, 0
	s_add_u32 s18, s18, 0x80
	s_addc_u32 s19, s19, 0
	v_mfma_f32_16x16x32_bf16 v[148:151], v[196:199], v[164:167], v[148:151]
	s_add_u32 s20, s20, 0xa000
	s_sub_u32 s22, s20, 0x1e000
	s_cmp_ge_u32 s20, 0x1e000
	s_cselect_b32 s20, s22, s20
	v_mfma_f32_16x16x32_bf16 v[152:155], v[196:199], v[168:171], v[152:155]
	v_add_u32_e32 v10, s21, v8
	v_add_u32_e32 v12, s21, v9
	v_xor_b32_e32 v11, 64, v10
	v_xor_b32_e32 v13, 64, v12
	v_mfma_f32_16x16x32_bf16 v[156:159], v[196:199], v[172:175], v[156:159]
	s_add_u32 s21, s21, 0xa000
	s_sub_u32 s23, s21, 0x1e000
	s_cmp_ge_u32 s21, 0x1e000
	s_cselect_b32 s21, s23, s21
	s_waitcnt vmcnt(10) lgkmcnt(0)
	s_barrier
	v_mfma_f32_16x16x32_bf16 v[64:67], v[216:219], v[200:203], v[64:67]
	ds_read_b128 v[160:163], v10 offset:0
	v_mfma_f32_16x16x32_bf16 v[68:71], v[216:219], v[204:207], v[68:71]
	s_add_u32 m0, s20, 0x0
	v_mfma_f32_16x16x32_bf16 v[72:75], v[216:219], v[208:211], v[72:75]
	ds_read_b128 v[164:167], v10 offset:2048
	v_mfma_f32_16x16x32_bf16 v[76:79], v[216:219], v[212:215], v[76:79]
	global_load_lds_dwordx4 v2, s[16:17]
	v_mfma_f32_16x16x32_bf16 v[80:83], v[220:223], v[200:203], v[80:83]
	ds_read_b128 v[168:171], v10 offset:4096
	v_mfma_f32_16x16x32_bf16 v[84:87], v[220:223], v[204:207], v[84:87]
	s_add_u32 m0, s20, 0x1000
	v_mfma_f32_16x16x32_bf16 v[88:91], v[220:223], v[208:211], v[88:91]
	ds_read_b128 v[172:175], v10 offset:6144
	v_mfma_f32_16x16x32_bf16 v[92:95], v[220:223], v[212:215], v[92:95]
	global_load_lds_dwordx4 v3, s[16:17]
	v_mfma_f32_16x16x32_bf16 v[96:99], v[224:227], v[200:203], v[96:99]
	ds_read_b128 v[176:179], v12 offset:0
	v_mfma_f32_16x16x32_bf16 v[100:103], v[224:227], v[204:207], v[100:103]
	s_add_u32 m0, s20, 0x2000
	v_mfma_f32_16x16x32_bf16 v[104:107], v[224:227], v[208:211], v[104:107]
	ds_read_b128 v[180:183], v12 offset:2048
	v_mfma_f32_16x16x32_bf16 v[108:111], v[224:227], v[212:215], v[108:111]
	global_load_lds_dwordx4 v4, s[16:17]
	v_mfma_f32_16x16x32_bf16 v[112:115], v[228:231], v[200:203], v[112:115]
	ds_read_b128 v[184:187], v12 offset:4096
	v_mfma_f32_16x16x32_bf16 v[116:119], v[228:231], v[204:207], v[116:119]
	s_add_u32 m0, s20, 0x3000
	v_mfma_f32_16x16x32_bf16 v[120:123], v[228:231], v[208:211], v[120:123]
	ds_read_b128 v[188:191], v12 offset:6144
	v_mfma_f32_16x16x32_bf16 v[124:127], v[228:231], v[212:215], v[124:127]
	global_load_lds_dwordx4 v5, s[16:17]
	v_mfma_f32_16x16x32_bf16 v[128:131], v[232:235], v[200:203], v[128:131]
	ds_read_b128 v[192:195], v12 offset:8192
	v_mfma_f32_16x16x32_bf16 v[132:135], v[232:235], v[204:207], v[132:135]
	s_add_u32 m0, s20, 0x4000
	v_mfma_f32_16x16x32_bf16 v[136:139], v[232:235], v[208:211], v[136:139]
	ds_read_b128 v[196:199], v12 offset:10240
	v_mfma_f32_16x16x32_bf16 v[140:143], v[232:235], v[212:215], v[140:143]
	global_load_lds_dwordx4 v2, s[18:19]
	v_mfma_f32_16x16x32_bf16 v[144:147], v[236:239], v[200:203], v[144:147]
	v_mfma_f32_16x16x32_bf16 v[148:151], v[236:239], v[204:207], v[148:151]
	v_mfma_f32_16x16x32_bf16 v[152:155], v[236:239], v[208:211], v[152:155]
	v_mfma_f32_16x16x32_bf16 v[156:159], v[236:239], v[212:215], v[156:159]
	s_add_u32 s15, s15, 1
	s_cmp_lt_u32 s15, 9
	s_cbranch_scc1 .Lou_loop
	s_waitcnt lgkmcnt(0)
	v_mfma_f32_16x16x32_bf16 v[64:67], v[176:179], v[160:163], v[64:67]
	ds_read_b128 v[200:203], v11 offset:0
	v_mfma_f32_16x16x32_bf16 v[68:71], v[176:179], v[164:167], v[68:71]
	s_add_u32 m0, s20, 0x5000
	v_mfma_f32_16x16x32_bf16 v[72:75], v[176:179], v[168:171], v[72:75]
	ds_read_b128 v[204:207], v11 offset:2048
	v_mfma_f32_16x16x32_bf16 v[76:79], v[176:179], v[172:175], v[76:79]
	global_load_lds_dwordx4 v3, s[18:19]
	v_mfma_f32_16x16x32_bf16 v[80:83], v[180:183], v[160:163], v[80:83]
	ds_read_b128 v[208:211], v11 offset:4096
	v_mfma_f32_16x16x32_bf16 v[84:87], v[180:183], v[164:167], v[84:87]
	s_add_u32 m0, s20, 0x6000
	v_mfma_f32_16x16x32_bf16 v[88:91], v[180:183], v[168:171], v[88:91]
	ds_read_b128 v[212:215], v11 offset:6144
	v_mfma_f32_16x16x32_bf16 v[92:95], v[180:183], v[172:175], v[92:95]
	global_load_lds_dwordx4 v4, s[18:19]
	v_mfma_f32_16x16x32_bf16 v[96:99], v[184:187], v[160:163], v[96:99]
	ds_read_b128 v[216:219], v13 offset:0
	v_mfma_f32_16x16x32_bf16 v[100:103], v[184:187], v[164:167], v[100:103]
	s_add_u32 m0, s20, 0x7000
	v_mfma_f32_16x16x32_bf16 v[104:107], v[184:187], v[168:171], v[104:107]
	ds_read_b128 v[220:223], v13 offset:2048
	v_mfma_f32_16x16x32_bf16 v[108:111], v[184:187], v[172:175], v[108:111]
	global_load_lds_dwordx4 v5, s[18:19]
	v_mfma_f32_16x16x32_bf16 v[112:115], v[188:191], v[160:163], v[112:115]
	ds_read_b128 v[224:227], v13 offset:4096
	v_mfma_f32_16x16x32_bf16 v[116:119], v[188:191], v[164:167], v[116:119]
	s_add_u32 m0, s20, 0x8000
	v_mfma_f32_16x16x32_bf16 v[120:123], v[188:191], v[168:171], v[120:123]
	ds_read_b128 v[228:231], v13 offset:6144
	v_mfma_f32_16x16x32_bf16 v[124:127], v[188:191], v[172:175], v[124:127]
	global_load_lds_dwordx4 v6, s[18:19]
	v_mfma_f32_16x16x32_bf16 v[128:131], v[192:195], v[160:163], v[128:131]
	ds_read_b128 v[232:235], v13 offset:8192
	v_mfma_f32_16x16x32_bf16 v[132:135], v[192:195], v[164:167], v[132:135]
	s_add_u32 m0, s20, 0x9000
	v_mfma_f32_16x16x32_bf16 v[136:139], v[192:195], v[168:171], v[136:139]
	ds_read_b128 v[236:239], v13 offset:10240
	v_mfma_f32_16x16x32_bf16 v[140:143], v[192:195], v[172:175], v[140:143]
	global_load_lds_dwordx4 v7, s[18:19]
	v_mfma_f32_16x16x32_bf16 v[144:147], v[196:199], v[160:163], v[144:147]
	s_add_u32 s16, s16, 0x80
	s_addc_u32 s17, s17, 0
	s_add_u32 s18, s18, 0x80
	s_addc_u32 s19, s19, 0
	v_mfma_f32_16x16x32_bf16 v[148:151], v[196:199], v[164:167], v[148:151]
	s_add_u32 s20, s20, 0xa000
	s_sub_u32 s22, s20, 0x1e000
	s_cmp_ge_u32 s20, 0x1e000
	s_cselect_b32 s20, s22, s20
	v_mfma_f32_16x16x32_bf16 v[152:155], v[196:199], v[168:171], v[152:155]
	v_add_u32_e32 v10, s21, v8
	v_add_u32_e32 v12, s21, v9
	v_xor_b32_e32 v11, 64, v10
	v_xor_b32_e32 v13, 64, v12
	v_mfma_f32_16x16x32_bf16 v[156:159], v[196:199], v[172:175], v[156:159]
	s_add_u32 s21, s21, 0xa000
	s_sub_u32 s23, s21, 0x1e000
	s_cmp_ge_u32 s21, 0x1e000
	s_cselect_b32 s21, s23, s21
	s_waitcnt vmcnt(10) lgkmcnt(0)
	s_barrier
	v_mfma_f32_16x16x32_bf16 v[64:67], v[216:219], v[200:203], v[64:67]
	ds_read_b128 v[160:163], v10 offset:0
	v_mfma_f32_16x16x32_bf16 v[68:71], v[216:219], v[204:207], v[68:71]
	ds_read_b128 v[164:167], v10 offset:2048
	v_mfma_f32_16x16x32_bf16 v[72:75], v[216:219], v[208:211], v[72:75]
	ds_read_b128 v[168:171], v10 offset:4096
	v_mfma_f32_16x16x32_bf16 v[76:79], v[216:219], v[212:215], v[76:79]
	ds_read_b128 v[172:175], v10 offset:6144
	v_mfma_f32_16x16x32_bf16 v[80:83], v[220:223], v[200:203], v[80:83]
	ds_read_b128 v[176:179], v12 offset:0
	v_mfma_f32_16x16x32_bf16 v[84:87], v[220:223], v[204:207], v[84:87]
	ds_read_b128 v[180:183], v12 offset:2048
	v_mfma_f32_16x16x32_bf16 v[88:91], v[220:223], v[208:211], v[88:91]
	ds_read_b128 v[184:187], v12 offset:4096
	v_mfma_f32_16x16x32_bf16 v[92:95], v[220:223], v[212:215], v[92:95]
	ds_read_b128 v[188:191], v12 offset:6144
	v_mfma_f32_16x16x32_bf16 v[96:99], v[224:227], v[200:203], v[96:99]
	ds_read_b128 v[192:195], v12 offset:8192
	v_mfma_f32_16x16x32_bf16 v[100:103], v[224:227], v[204:207], v[100:103]
	ds_read_b128 v[196:199], v12 offset:10240
	v_mfma_f32_16x16x32_bf16 v[104:107], v[224:227], v[208:211], v[104:107]
	v_mfma_f32_16x16x32_bf16 v[108:111], v[224:227], v[212:215], v[108:111]
	v_mfma_f32_16x16x32_bf16 v[112:115], v[228:231], v[200:203], v[112:115]
	v_mfma_f32_16x16x32_bf16 v[116:119], v[228:231], v[204:207], v[116:119]
	v_mfma_f32_16x16x32_bf16 v[120:123], v[228:231], v[208:211], v[120:123]
	v_mfma_f32_16x16x32_bf16 v[124:127], v[228:231], v[212:215], v[124:127]
	v_mfma_f32_16x16x32_bf16 v[128:131], v[232:235], v[200:203], v[128:131]
	v_mfma_f32_16x16x32_bf16 v[132:135], v[232:235], v[204:207], v[132:135]
	v_mfma_f32_16x16x32_bf16 v[136:139], v[232:235], v[208:211], v[136:139]
	v_mfma_f32_16x16x32_bf16 v[140:143], v[232:235], v[212:215], v[140:143]
	v_mfma_f32_16x16x32_bf16 v[144:147], v[236:239], v[200:203], v[144:147]
	v_mfma_f32_16x16x32_bf16 v[148:151], v[236:239], v[204:207], v[148:151]
	v_mfma_f32_16x16x32_bf16 v[152:155], v[236:239], v[208:211], v[152:155]
	v_mfma_f32_16x16x32_bf16 v[156:159], v[236:239], v[212:215], v[156:159]
	s_waitcnt lgkmcnt(0)
	v_mfma_f32_16x16x32_bf16 v[64:67], v[176:179], v[160:163], v[64:67]
	ds_read_b128 v[200:203], v11 offset:0
	v_mfma_f32_16x16x32_bf16 v[68:71], v[176:179], v[164:167], v[68:71]
	ds_read_b128 v[204:207], v11 offset:2048
	v_mfma_f32_16x16x32_bf16 v[72:75], v[176:179], v[168:171], v[72:75]
	ds_read_b128 v[208:211], v11 offset:4096
	v_mfma_f32_16x16x32_bf16 v[76:79], v[176:179], v[172:175], v[76:79]
	ds_read_b128 v[212:215], v11 offset:6144
	v_mfma_f32_16x16x32_bf16 v[80:83], v[180:183], v[160:163], v[80:83]
	ds_read_b128 v[216:219], v13 offset:0
	v_mfma_f32_16x16x32_bf16 v[84:87], v[180:183], v[164:167], v[84:87]
	ds_read_b128 v[220:223], v13 offset:2048
	v_mfma_f32_16x16x32_bf16 v[88:91], v[180:183], v[168:171], v[88:91]
	ds_read_b128 v[224:227], v13 offset:4096
	v_mfma_f32_16x16x32_bf16 v[92:95], v[180:183], v[172:175], v[92:95]
	ds_read_b128 v[228:231], v13 offset:6144
	v_mfma_f32_16x16x32_bf16 v[96:99], v[184:187], v[160:163], v[96:99]
	ds_read_b128 v[232:235], v13 offset:8192
	v_mfma_f32_16x16x32_bf16 v[100:103], v[184:187], v[164:167], v[100:103]
	ds_read_b128 v[236:239], v13 offset:10240
	v_mfma_f32_16x16x32_bf16 v[104:107], v[184:187], v[168:171], v[104:107]
	v_mfma_f32_16x16x32_bf16 v[108:111], v[184:187], v[172:175], v[108:111]
	v_mfma_f32_16x16x32_bf16 v[112:115], v[188:191], v[160:163], v[112:115]
	v_mfma_f32_16x16x32_bf16 v[116:119], v[188:191], v[164:167], v[116:119]
	v_mfma_f32_16x16x32_bf16 v[120:123], v[188:191], v[168:171], v[120:123]
	v_mfma_f32_16x16x32_bf16 v[124:127], v[188:191], v[172:175], v[124:127]
	v_mfma_f32_16x16x32_bf16 v[128:131], v[192:195], v[160:163], v[128:131]
	v_mfma_f32_16x16x32_bf16 v[132:135], v[192:195], v[164:167], v[132:135]
	v_mfma_f32_16x16x32_bf16 v[136:139], v[192:195], v[168:171], v[136:139]
	v_mfma_f32_16x16x32_bf16 v[140:143], v[192:195], v[172:175], v[140:143]
	v_mfma_f32_16x16x32_bf16 v[144:147], v[196:199], v[160:163], v[144:147]
	v_add_u32_e32 v10, s21, v8
	v_add_u32_e32 v12, s21, v9
	v_xor_b32_e32 v11, 64, v10
	v_xor_b32_e32 v13, 64, v12
	v_mfma_f32_16x16x32_bf16 v[148:151], v[196:199], v[164:167], v[148:151]
	s_add_u32 s21, s21, 0xa000
	s_sub_u32 s23, s21, 0x1e000
	s_cmp_ge_u32 s21, 0x1e000
	s_cselect_b32 s21, s23, s21
	v_mfma_f32_16x16x32_bf16 v[152:155], v[196:199], v[168:171], v[152:155]
	v_mfma_f32_16x16x32_bf16 v[156:159], v[196:199], v[172:175], v[156:159]
	s_waitcnt vmcnt(0) lgkmcnt(0)
	s_barrier
	v_mfma_f32_16x16x32_bf16 v[64:67], v[216:219], v[200:203], v[64:67]
	ds_read_b128 v[160:163], v10 offset:0
	v_mfma_f32_16x16x32_bf16 v[68:71], v[216:219], v[204:207], v[68:71]
	global_load_dwordx4 v[16:19], v56, s[8:9] offset:0
	v_mfma_f32_16x16x32_bf16 v[72:75], v[216:219], v[208:211], v[72:75]
	ds_read_b128 v[164:167], v10 offset:2048
	v_mfma_f32_16x16x32_bf16 v[76:79], v[216:219], v[212:215], v[76:79]
	global_load_dwordx4 v[20:23], v57, s[8:9] offset:0
	v_mfma_f32_16x16x32_bf16 v[80:83], v[220:223], v[200:203], v[80:83]
	ds_read_b128 v[168:171], v10 offset:4096
	v_mfma_f32_16x16x32_bf16 v[84:87], v[220:223], v[204:207], v[84:87]
	global_load_dwordx4 v[24:27], v58, s[8:9] offset:0
	v_mfma_f32_16x16x32_bf16 v[88:91], v[220:223], v[208:211], v[88:91]
	ds_read_b128 v[172:175], v10 offset:6144
	v_mfma_f32_16x16x32_bf16 v[92:95], v[220:223], v[212:215], v[92:95]
	global_load_dwordx4 v[28:31], v59, s[8:9] offset:0
	v_mfma_f32_16x16x32_bf16 v[96:99], v[224:227], v[200:203], v[96:99]
	ds_read_b128 v[176:179], v12 offset:0
	v_mfma_f32_16x16x32_bf16 v[100:103], v[224:227], v[204:207], v[100:103]
	global_load_dwordx4 v[32:35], v56, s[8:9] offset:64
	v_mfma_f32_16x16x32_bf16 v[104:107], v[224:227], v[208:211], v[104:107]
	ds_read_b128 v[180:183], v12 offset:2048
	v_mfma_f32_16x16x32_bf16 v[108:111], v[224:227], v[212:215], v[108:111]
	global_load_dwordx4 v[36:39], v57, s[8:9] offset:64
	v_mfma_f32_16x16x32_bf16 v[112:115], v[228:231], v[200:203], v[112:115]
	ds_read_b128 v[184:187], v12 offset:4096
	v_mfma_f32_16x16x32_bf16 v[116:119], v[228:231], v[204:207], v[116:119]
	global_load_dwordx4 v[40:43], v58, s[8:9] offset:64
	v_mfma_f32_16x16x32_bf16 v[120:123], v[228:231], v[208:211], v[120:123]
	ds_read_b128 v[188:191], v12 offset:6144
	v_mfma_f32_16x16x32_bf16 v[124:127], v[228:231], v[212:215], v[124:127]
	global_load_dwordx4 v[44:47], v59, s[8:9] offset:64
	v_mfma_f32_16x16x32_bf16 v[128:131], v[232:235], v[200:203], v[128:131]
	ds_read_b128 v[192:195], v12 offset:8192
	v_mfma_f32_16x16x32_bf16 v[132:135], v[232:235], v[204:207], v[132:135]
	global_load_dwordx4 v[48:51], v56, s[8:9] offset:128
	v_mfma_f32_16x16x32_bf16 v[136:139], v[232:235], v[208:211], v[136:139]
	ds_read_b128 v[196:199], v12 offset:10240
	v_mfma_f32_16x16x32_bf16 v[140:143], v[232:235], v[212:215], v[140:143]
	global_load_dwordx4 v[52:55], v57, s[8:9] offset:128
	v_mfma_f32_16x16x32_bf16 v[144:147], v[236:239], v[200:203], v[144:147]
	global_load_dwordx4 v[240:243], v58, s[8:9] offset:128
	v_mfma_f32_16x16x32_bf16 v[148:151], v[236:239], v[204:207], v[148:151]
	global_load_dwordx4 v[244:247], v59, s[8:9] offset:128
	v_mfma_f32_16x16x32_bf16 v[152:155], v[236:239], v[208:211], v[152:155]
	global_load_dwordx4 v[248:251], v56, s[8:9] offset:192
	v_mfma_f32_16x16x32_bf16 v[156:159], v[236:239], v[212:215], v[156:159]
	global_load_dwordx4 v[252:255], v57, s[8:9] offset:192
	s_waitcnt lgkmcnt(0)
	v_mfma_f32_16x16x32_bf16 v[64:67], v[176:179], v[160:163], v[64:67]
	ds_read_b128 v[200:203], v11 offset:0
	v_mfma_f32_16x16x32_bf16 v[68:71], v[176:179], v[164:167], v[68:71]
	ds_read_b128 v[204:207], v11 offset:2048
	v_mfma_f32_16x16x32_bf16 v[72:75], v[176:179], v[168:171], v[72:75]
	ds_read_b128 v[208:211], v11 offset:4096
	v_mfma_f32_16x16x32_bf16 v[76:79], v[176:179], v[172:175], v[76:79]
	ds_read_b128 v[212:215], v11 offset:6144
	v_mfma_f32_16x16x32_bf16 v[80:83], v[180:183], v[160:163], v[80:83]
	ds_read_b128 v[216:219], v13 offset:0
	v_mfma_f32_16x16x32_bf16 v[84:87], v[180:183], v[164:167], v[84:87]
	ds_read_b128 v[220:223], v13 offset:2048
	v_mfma_f32_16x16x32_bf16 v[88:91], v[180:183], v[168:171], v[88:91]
	ds_read_b128 v[224:227], v13 offset:4096
	v_mfma_f32_16x16x32_bf16 v[92:95], v[180:183], v[172:175], v[92:95]
	ds_read_b128 v[228:231], v13 offset:6144
	v_mfma_f32_16x16x32_bf16 v[96:99], v[184:187], v[160:163], v[96:99]
	ds_read_b128 v[232:235], v13 offset:8192
	v_mfma_f32_16x16x32_bf16 v[100:103], v[184:187], v[164:167], v[100:103]
	ds_read_b128 v[236:239], v13 offset:10240
	v_mfma_f32_16x16x32_bf16 v[104:107], v[184:187], v[168:171], v[104:107]
	v_mfma_f32_16x16x32_bf16 v[108:111], v[184:187], v[172:175], v[108:111]
	v_mfma_f32_16x16x32_bf16 v[112:115], v[188:191], v[160:163], v[112:115]
	v_mfma_f32_16x16x32_bf16 v[116:119], v[188:191], v[164:167], v[116:119]
	v_mfma_f32_16x16x32_bf16 v[120:123], v[188:191], v[168:171], v[120:123]
	v_mfma_f32_16x16x32_bf16 v[124:127], v[188:191], v[172:175], v[124:127]
	v_mfma_f32_16x16x32_bf16 v[128:131], v[192:195], v[160:163], v[128:131]
	v_mfma_f32_16x16x32_bf16 v[132:135], v[192:195], v[164:167], v[132:135]
	v_mfma_f32_16x16x32_bf16 v[136:139], v[192:195], v[168:171], v[136:139]
	v_mfma_f32_16x16x32_bf16 v[140:143], v[192:195], v[172:175], v[140:143]
	v_mfma_f32_16x16x32_bf16 v[144:147], v[196:199], v[160:163], v[144:147]
	v_mfma_f32_16x16x32_bf16 v[148:151], v[196:199], v[164:167], v[148:151]
	v_mfma_f32_16x16x32_bf16 v[152:155], v[196:199], v[168:171], v[152:155]
	v_mfma_f32_16x16x32_bf16 v[156:159], v[196:199], v[172:175], v[156:159]
	s_waitcnt lgkmcnt(0)
	v_mfma_f32_16x16x32_bf16 v[64:67], v[216:219], v[200:203], v[64:67]
	v_mfma_f32_16x16x32_bf16 v[68:71], v[216:219], v[204:207], v[68:71]
	global_load_dwordx4 v[160:163], v58, s[8:9] offset:192
	v_mfma_f32_16x16x32_bf16 v[72:75], v[216:219], v[208:211], v[72:75]
	v_mfma_f32_16x16x32_bf16 v[76:79], v[216:219], v[212:215], v[76:79]
	global_load_dwordx4 v[164:167], v59, s[8:9] offset:192
	v_mfma_f32_16x16x32_bf16 v[80:83], v[220:223], v[200:203], v[80:83]
	v_mfma_f32_16x16x32_bf16 v[84:87], v[220:223], v[204:207], v[84:87]
	global_load_dwordx4 v[168:171], v56, s[8:9] offset:256
	v_mfma_f32_16x16x32_bf16 v[88:91], v[220:223], v[208:211], v[88:91]
	v_mfma_f32_16x16x32_bf16 v[92:95], v[220:223], v[212:215], v[92:95]
	global_load_dwordx4 v[172:175], v57, s[8:9] offset:256
	v_mfma_f32_16x16x32_bf16 v[96:99], v[224:227], v[200:203], v[96:99]
	v_mfma_f32_16x16x32_bf16 v[100:103], v[224:227], v[204:207], v[100:103]
	global_load_dwordx4 v[176:179], v58, s[8:9] offset:256
	v_mfma_f32_16x16x32_bf16 v[104:107], v[224:227], v[208:211], v[104:107]
	v_mfma_f32_16x16x32_bf16 v[108:111], v[224:227], v[212:215], v[108:111]
	global_load_dwordx4 v[180:183], v59, s[8:9] offset:256
	v_mfma_f32_16x16x32_bf16 v[112:115], v[228:231], v[200:203], v[112:115]
	v_mfma_f32_16x16x32_bf16 v[116:119], v[228:231], v[204:207], v[116:119]
	global_load_dwordx4 v[184:187], v56, s[8:9] offset:320
	v_mfma_f32_16x16x32_bf16 v[120:123], v[228:231], v[208:211], v[120:123]
	v_mfma_f32_16x16x32_bf16 v[124:127], v[228:231], v[212:215], v[124:127]
	global_load_dwordx4 v[188:191], v57, s[8:9] offset:320
	v_mfma_f32_16x16x32_bf16 v[128:131], v[232:235], v[200:203], v[128:131]
	v_mfma_f32_16x16x32_bf16 v[132:135], v[232:235], v[204:207], v[132:135]
	global_load_dwordx4 v[192:195], v58, s[8:9] offset:320
	v_mfma_f32_16x16x32_bf16 v[136:139], v[232:235], v[208:211], v[136:139]
	v_mfma_f32_16x16x32_bf16 v[140:143], v[232:235], v[212:215], v[140:143]
	global_load_dwordx4 v[196:199], v59, s[8:9] offset:320
	v_mfma_f32_16x16x32_bf16 v[144:147], v[236:239], v[200:203], v[144:147]
	v_mfma_f32_16x16x32_bf16 v[148:151], v[236:239], v[204:207], v[148:151]
	v_mfma_f32_16x16x32_bf16 v[152:155], v[236:239], v[208:211], v[152:155]
	v_mfma_f32_16x16x32_bf16 v[156:159], v[236:239], v[212:215], v[156:159]
	v_and_b32_e32 v12, 63, v0
	v_cmp_gt_u32_e32 vcc, 16, v12
	v_xor_b32_e32 v13, 16, v12
	v_lshlrev_b32_e32 v13, 2, v13
	v_xor_b32_e32 v12, 32, v12
	v_lshlrev_b32_e32 v12, 2, v12
	v_bfe_u32 v14, v0, 6, 1
	v_mul_u32_u24_e32 v14, 0x60, v14
	v_bfe_u32 v15, v0, 4, 2
	v_lshl_add_u32 v14, v15, 2, v14
	v_add_u32_e32 v14, s13, v14
	v_lshlrev_b32_e32 v14, 2, v14
	global_load_dwordx4 v[200:203], v14, s[24:25]
	global_load_dwordx4 v[204:207], v14, s[24:25] offset:64
	global_load_dwordx4 v[208:211], v14, s[24:25] offset:128
	global_load_dwordx4 v[212:215], v14, s[24:25] offset:192
	global_load_dwordx4 v[216:219], v14, s[24:25] offset:256
	global_load_dwordx4 v[220:223], v14, s[24:25] offset:320
	v_lshrrev_b32_e32 v60, 1, v56
	v_lshrrev_b32_e32 v61, 1, v57
	v_lshrrev_b32_e32 v62, 1, v58
	v_lshrrev_b32_e32 v63, 1, v59
	v_bfe_u32 v8, v0, 7, 1
	v_and_b32_e32 v9, 15, v0
	v_lshl_add_u32 v8, v8, 6, v9
	v_add_u32_e32 v8, s12, v8
	v_lshlrev_b32_e32 v8, 6, v8
	v_bfe_u32 v9, v0, 6, 1
	v_lshlrev_b32_e32 v9, 1, v9
	v_add_u32_e32 v9, s30, v9
	v_lshl_add_u32 v8, v9, 2, v8
	v_add_u32_e32 v9, 0x400, v8
	v_add_u32_e32 v10, 0x400, v9
	v_add_u32_e32 v11, 0x400, v10
	s_waitcnt vmcnt(0)
	v_pk_add_f32 v[64:65], v[64:65], v[16:17]
	v_pk_add_f32 v[66:67], v[66:67], v[18:19]
	global_store_dwordx4 v56, v[64:67], s[10:11]
	v_pk_mul_f32 v[224:225], v[200:201], v[64:65]
	v_pk_mul_f32 v[226:227], v[202:203], v[66:67]
	v_cvt_pk_bf16_f32 v228, v224, v225
	v_cvt_pk_bf16_f32 v229, v226, v227
	global_store_dwordx2 v60, v[228:229], s[28:29]
	v_pk_mul_f32 v[230:231], v[64:65], v[64:65]
	v_pk_mul_f32 v[232:233], v[66:67], v[66:67]
	v_add_f32_e32 v230, v230, v231
	v_add_f32_e32 v230, v232, v230
	v_add_f32_e32 v234, v233, v230
	v_pk_add_f32 v[80:81], v[80:81], v[32:33]
	v_pk_add_f32 v[82:83], v[82:83], v[34:35]
	global_store_dwordx4 v56, v[80:83], s[10:11] offset:64
	v_pk_mul_f32 v[224:225], v[204:205], v[80:81]
	v_pk_mul_f32 v[226:227], v[206:207], v[82:83]
	v_cvt_pk_bf16_f32 v228, v224, v225
	v_cvt_pk_bf16_f32 v229, v226, v227
	global_store_dwordx2 v60, v[228:229], s[28:29] offset:32
	v_pk_mul_f32 v[230:231], v[80:81], v[80:81]
	v_pk_mul_f32 v[232:233], v[82:83], v[82:83]
	v_add_f32_e32 v230, v230, v231
	v_add_f32_e32 v230, v232, v230
	v_add_f32_e32 v230, v233, v230
	v_add_f32_e32 v234, v234, v230
	v_pk_add_f32 v[96:97], v[96:97], v[48:49]
	v_pk_add_f32 v[98:99], v[98:99], v[50:51]
	global_store_dwordx4 v56, v[96:99], s[10:11] offset:128
	v_pk_mul_f32 v[224:225], v[208:209], v[96:97]
	v_pk_mul_f32 v[226:227], v[210:211], v[98:99]
	v_cvt_pk_bf16_f32 v228, v224, v225
	v_cvt_pk_bf16_f32 v229, v226, v227
	global_store_dwordx2 v60, v[228:229], s[28:29] offset:64
	v_pk_mul_f32 v[230:231], v[96:97], v[96:97]
	v_pk_mul_f32 v[232:233], v[98:99], v[98:99]
	v_add_f32_e32 v230, v230, v231
	v_add_f32_e32 v230, v232, v230
	v_add_f32_e32 v230, v233, v230
	v_add_f32_e32 v234, v234, v230
	v_pk_add_f32 v[112:113], v[112:113], v[248:249]
	v_pk_add_f32 v[114:115], v[114:115], v[250:251]
	global_store_dwordx4 v56, v[112:115], s[10:11] offset:192
	v_pk_mul_f32 v[224:225], v[212:213], v[112:113]
	v_pk_mul_f32 v[226:227], v[214:215], v[114:115]
	v_cvt_pk_bf16_f32 v228, v224, v225
	v_cvt_pk_bf16_f32 v229, v226, v227
	global_store_dwordx2 v60, v[228:229], s[28:29] offset:96
	v_pk_mul_f32 v[230:231], v[112:113], v[112:113]
	v_pk_mul_f32 v[232:233], v[114:115], v[114:115]
	v_add_f32_e32 v230, v230, v231
	v_add_f32_e32 v230, v232, v230
	v_add_f32_e32 v235, v233, v230
	v_pk_add_f32 v[128:129], v[128:129], v[168:169]
	v_pk_add_f32 v[130:131], v[130:131], v[170:171]
	global_store_dwordx4 v56, v[128:131], s[10:11] offset:256
	v_pk_mul_f32 v[224:225], v[216:217], v[128:129]
	v_pk_mul_f32 v[226:227], v[218:219], v[130:131]
	v_cvt_pk_bf16_f32 v228, v224, v225
	v_cvt_pk_bf16_f32 v229, v226, v227
	global_store_dwordx2 v60, v[228:229], s[28:29] offset:128
	v_pk_mul_f32 v[230:231], v[128:129], v[128:129]
	v_pk_mul_f32 v[232:233], v[130:131], v[130:131]
	v_add_f32_e32 v230, v230, v231
	v_add_f32_e32 v230, v232, v230
	v_add_f32_e32 v230, v233, v230
	v_add_f32_e32 v235, v235, v230
	v_pk_add_f32 v[144:145], v[144:145], v[184:185]
	v_pk_add_f32 v[146:147], v[146:147], v[186:187]
	global_store_dwordx4 v56, v[144:147], s[10:11] offset:320
	v_pk_mul_f32 v[224:225], v[220:221], v[144:145]
	v_pk_mul_f32 v[226:227], v[222:223], v[146:147]
	v_cvt_pk_bf16_f32 v228, v224, v225
	v_cvt_pk_bf16_f32 v229, v226, v227
	global_store_dwordx2 v60, v[228:229], s[28:29] offset:160
	v_pk_mul_f32 v[230:231], v[144:145], v[144:145]
	v_pk_mul_f32 v[232:233], v[146:147], v[146:147]
	v_add_f32_e32 v230, v230, v231
	v_add_f32_e32 v230, v232, v230
	v_add_f32_e32 v230, v233, v230
	v_add_f32_e32 v235, v235, v230
	v_pk_add_f32 v[68:69], v[68:69], v[20:21]
	v_pk_add_f32 v[70:71], v[70:71], v[22:23]
	global_store_dwordx4 v57, v[68:71], s[10:11]
	v_pk_mul_f32 v[224:225], v[200:201], v[68:69]
	v_pk_mul_f32 v[226:227], v[202:203], v[70:71]
	v_cvt_pk_bf16_f32 v228, v224, v225
	v_cvt_pk_bf16_f32 v229, v226, v227
	global_store_dwordx2 v61, v[228:229], s[28:29]
	v_pk_mul_f32 v[230:231], v[68:69], v[68:69]
	v_pk_mul_f32 v[232:233], v[70:71], v[70:71]
	v_add_f32_e32 v230, v230, v231
	v_add_f32_e32 v230, v232, v230
	v_add_f32_e32 v236, v233, v230
	v_pk_add_f32 v[84:85], v[84:85], v[36:37]
	v_pk_add_f32 v[86:87], v[86:87], v[38:39]
	global_store_dwordx4 v57, v[84:87], s[10:11] offset:64
	v_pk_mul_f32 v[224:225], v[204:205], v[84:85]
	v_pk_mul_f32 v[226:227], v[206:207], v[86:87]
	v_cvt_pk_bf16_f32 v228, v224, v225
	v_cvt_pk_bf16_f32 v229, v226, v227
	global_store_dwordx2 v61, v[228:229], s[28:29] offset:32
	v_pk_mul_f32 v[230:231], v[84:85], v[84:85]
	v_pk_mul_f32 v[232:233], v[86:87], v[86:87]
	v_add_f32_e32 v230, v230, v231
	v_add_f32_e32 v230, v232, v230
	v_add_f32_e32 v230, v233, v230
	v_add_f32_e32 v236, v236, v230
	v_pk_add_f32 v[100:101], v[100:101], v[52:53]
	v_pk_add_f32 v[102:103], v[102:103], v[54:55]
	global_store_dwordx4 v57, v[100:103], s[10:11] offset:128
	v_pk_mul_f32 v[224:225], v[208:209], v[100:101]
	v_pk_mul_f32 v[226:227], v[210:211], v[102:103]
	v_cvt_pk_bf16_f32 v228, v224, v225
	v_cvt_pk_bf16_f32 v229, v226, v227
	global_store_dwordx2 v61, v[228:229], s[28:29] offset:64
	v_pk_mul_f32 v[230:231], v[100:101], v[100:101]
	v_pk_mul_f32 v[232:233], v[102:103], v[102:103]
	v_add_f32_e32 v230, v230, v231
	v_add_f32_e32 v230, v232, v230
	v_add_f32_e32 v230, v233, v230
	v_add_f32_e32 v236, v236, v230
	v_pk_add_f32 v[116:117], v[116:117], v[252:253]
	v_pk_add_f32 v[118:119], v[118:119], v[254:255]
	global_store_dwordx4 v57, v[116:119], s[10:11] offset:192
	v_pk_mul_f32 v[224:225], v[212:213], v[116:117]
	v_pk_mul_f32 v[226:227], v[214:215], v[118:119]
	v_cvt_pk_bf16_f32 v228, v224, v225
	v_cvt_pk_bf16_f32 v229, v226, v227
	global_store_dwordx2 v61, v[228:229], s[28:29] offset:96
	v_pk_mul_f32 v[230:231], v[116:117], v[116:117]
	v_pk_mul_f32 v[232:233], v[118:119], v[118:119]
	v_add_f32_e32 v230, v230, v231
	v_add_f32_e32 v230, v232, v230
	v_add_f32_e32 v237, v233, v230
	v_pk_add_f32 v[132:133], v[132:133], v[172:173]
	v_pk_add_f32 v[134:135], v[134:135], v[174:175]
	global_store_dwordx4 v57, v[132:135], s[10:11] offset:256
	v_pk_mul_f32 v[224:225], v[216:217], v[132:133]
	v_pk_mul_f32 v[226:227], v[218:219], v[134:135]
	v_cvt_pk_bf16_f32 v228, v224, v225
	v_cvt_pk_bf16_f32 v229, v226, v227
	global_store_dwordx2 v61, v[228:229], s[28:29] offset:128
	v_pk_mul_f32 v[230:231], v[132:133], v[132:133]
	v_pk_mul_f32 v[232:233], v[134:135], v[134:135]
	v_add_f32_e32 v230, v230, v231
	v_add_f32_e32 v230, v232, v230
	v_add_f32_e32 v230, v233, v230
	v_add_f32_e32 v237, v237, v230
	v_pk_add_f32 v[148:149], v[148:149], v[188:189]
	v_pk_add_f32 v[150:151], v[150:151], v[190:191]
	global_store_dwordx4 v57, v[148:151], s[10:11] offset:320
	v_pk_mul_f32 v[224:225], v[220:221], v[148:149]
	v_pk_mul_f32 v[226:227], v[222:223], v[150:151]
	v_cvt_pk_bf16_f32 v228, v224, v225
	v_cvt_pk_bf16_f32 v229, v226, v227
	global_store_dwordx2 v61, v[228:229], s[28:29] offset:160
	v_pk_mul_f32 v[230:231], v[148:149], v[148:149]
	v_pk_mul_f32 v[232:233], v[150:151], v[150:151]
	v_add_f32_e32 v230, v230, v231
	v_add_f32_e32 v230, v232, v230
	v_add_f32_e32 v230, v233, v230
	v_add_f32_e32 v237, v237, v230
	v_pk_add_f32 v[72:73], v[72:73], v[24:25]
	v_pk_add_f32 v[74:75], v[74:75], v[26:27]
	global_store_dwordx4 v58, v[72:75], s[10:11]
	v_pk_mul_f32 v[224:225], v[200:201], v[72:73]
	v_pk_mul_f32 v[226:227], v[202:203], v[74:75]
	v_cvt_pk_bf16_f32 v228, v224, v225
	v_cvt_pk_bf16_f32 v229, v226, v227
	global_store_dwordx2 v62, v[228:229], s[28:29]
	v_pk_mul_f32 v[230:231], v[72:73], v[72:73]
	v_pk_mul_f32 v[232:233], v[74:75], v[74:75]
	v_add_f32_e32 v230, v230, v231
	v_add_f32_e32 v230, v232, v230
	v_add_f32_e32 v238, v233, v230
	v_pk_add_f32 v[88:89], v[88:89], v[40:41]
	v_pk_add_f32 v[90:91], v[90:91], v[42:43]
	global_store_dwordx4 v58, v[88:91], s[10:11] offset:64
	v_pk_mul_f32 v[224:225], v[204:205], v[88:89]
	v_pk_mul_f32 v[226:227], v[206:207], v[90:91]
	v_cvt_pk_bf16_f32 v228, v224, v225
	v_cvt_pk_bf16_f32 v229, v226, v227
	global_store_dwordx2 v62, v[228:229], s[28:29] offset:32
	v_pk_mul_f32 v[230:231], v[88:89], v[88:89]
	v_pk_mul_f32 v[232:233], v[90:91], v[90:91]
	v_add_f32_e32 v230, v230, v231
	v_add_f32_e32 v230, v232, v230
	v_add_f32_e32 v230, v233, v230
	v_add_f32_e32 v238, v238, v230
	v_pk_add_f32 v[104:105], v[104:105], v[240:241]
	v_pk_add_f32 v[106:107], v[106:107], v[242:243]
	global_store_dwordx4 v58, v[104:107], s[10:11] offset:128
	v_pk_mul_f32 v[224:225], v[208:209], v[104:105]
	v_pk_mul_f32 v[226:227], v[210:211], v[106:107]
	v_cvt_pk_bf16_f32 v228, v224, v225
	v_cvt_pk_bf16_f32 v229, v226, v227
	global_store_dwordx2 v62, v[228:229], s[28:29] offset:64
	v_pk_mul_f32 v[230:231], v[104:105], v[104:105]
	v_pk_mul_f32 v[232:233], v[106:107], v[106:107]
	v_add_f32_e32 v230, v230, v231
	v_add_f32_e32 v230, v232, v230
	v_add_f32_e32 v230, v233, v230
	v_add_f32_e32 v238, v238, v230
	v_pk_add_f32 v[120:121], v[120:121], v[160:161]
	v_pk_add_f32 v[122:123], v[122:123], v[162:163]
	global_store_dwordx4 v58, v[120:123], s[10:11] offset:192
	v_pk_mul_f32 v[224:225], v[212:213], v[120:121]
	v_pk_mul_f32 v[226:227], v[214:215], v[122:123]
	v_cvt_pk_bf16_f32 v228, v224, v225
	v_cvt_pk_bf16_f32 v229, v226, v227
	global_store_dwordx2 v62, v[228:229], s[28:29] offset:96
	v_pk_mul_f32 v[230:231], v[120:121], v[120:121]
	v_pk_mul_f32 v[232:233], v[122:123], v[122:123]
	v_add_f32_e32 v230, v230, v231
	v_add_f32_e32 v230, v232, v230
	v_add_f32_e32 v239, v233, v230
	v_pk_add_f32 v[136:137], v[136:137], v[176:177]
	v_pk_add_f32 v[138:139], v[138:139], v[178:179]
	global_store_dwordx4 v58, v[136:139], s[10:11] offset:256
	v_pk_mul_f32 v[224:225], v[216:217], v[136:137]
	v_pk_mul_f32 v[226:227], v[218:219], v[138:139]
	v_cvt_pk_bf16_f32 v228, v224, v225
	v_cvt_pk_bf16_f32 v229, v226, v227
	global_store_dwordx2 v62, v[228:229], s[28:29] offset:128
	v_pk_mul_f32 v[230:231], v[136:137], v[136:137]
	v_pk_mul_f32 v[232:233], v[138:139], v[138:139]
	v_add_f32_e32 v230, v230, v231
	v_add_f32_e32 v230, v232, v230
	v_add_f32_e32 v230, v233, v230
	v_add_f32_e32 v239, v239, v230
	v_pk_add_f32 v[152:153], v[152:153], v[192:193]
	v_pk_add_f32 v[154:155], v[154:155], v[194:195]
	global_store_dwordx4 v58, v[152:155], s[10:11] offset:320
	v_pk_mul_f32 v[224:225], v[220:221], v[152:153]
	v_pk_mul_f32 v[226:227], v[222:223], v[154:155]
	v_cvt_pk_bf16_f32 v228, v224, v225
	v_cvt_pk_bf16_f32 v229, v226, v227
	global_store_dwordx2 v62, v[228:229], s[28:29] offset:160
	v_pk_mul_f32 v[230:231], v[152:153], v[152:153]
	v_pk_mul_f32 v[232:233], v[154:155], v[154:155]
	v_add_f32_e32 v230, v230, v231
	v_add_f32_e32 v230, v232, v230
	v_add_f32_e32 v230, v233, v230
	v_add_f32_e32 v239, v239, v230
	v_pk_add_f32 v[76:77], v[76:77], v[28:29]
	v_pk_add_f32 v[78:79], v[78:79], v[30:31]
	global_store_dwordx4 v59, v[76:79], s[10:11]
	v_pk_mul_f32 v[224:225], v[200:201], v[76:77]
	v_pk_mul_f32 v[226:227], v[202:203], v[78:79]
	v_cvt_pk_bf16_f32 v228, v224, v225
	v_cvt_pk_bf16_f32 v229, v226, v227
	global_store_dwordx2 v63, v[228:229], s[28:29]
	v_pk_mul_f32 v[230:231], v[76:77], v[76:77]
	v_pk_mul_f32 v[232:233], v[78:79], v[78:79]
	v_add_f32_e32 v230, v230, v231
	v_add_f32_e32 v230, v232, v230
	v_add_f32_e32 v14, v233, v230
	v_pk_add_f32 v[92:93], v[92:93], v[44:45]
	v_pk_add_f32 v[94:95], v[94:95], v[46:47]
	global_store_dwordx4 v59, v[92:95], s[10:11] offset:64
	v_pk_mul_f32 v[224:225], v[204:205], v[92:93]
	v_pk_mul_f32 v[226:227], v[206:207], v[94:95]
	v_cvt_pk_bf16_f32 v228, v224, v225
	v_cvt_pk_bf16_f32 v229, v226, v227
	global_store_dwordx2 v63, v[228:229], s[28:29] offset:32
	v_pk_mul_f32 v[230:231], v[92:93], v[92:93]
	v_pk_mul_f32 v[232:233], v[94:95], v[94:95]
	v_add_f32_e32 v230, v230, v231
	v_add_f32_e32 v230, v232, v230
	v_add_f32_e32 v230, v233, v230
	v_add_f32_e32 v14, v14, v230
	v_pk_add_f32 v[108:109], v[108:109], v[244:245]
	v_pk_add_f32 v[110:111], v[110:111], v[246:247]
	global_store_dwordx4 v59, v[108:111], s[10:11] offset:128
	v_pk_mul_f32 v[224:225], v[208:209], v[108:109]
	v_pk_mul_f32 v[226:227], v[210:211], v[110:111]
	v_cvt_pk_bf16_f32 v228, v224, v225
	v_cvt_pk_bf16_f32 v229, v226, v227
	global_store_dwordx2 v63, v[228:229], s[28:29] offset:64
	v_pk_mul_f32 v[230:231], v[108:109], v[108:109]
	v_pk_mul_f32 v[232:233], v[110:111], v[110:111]
	v_add_f32_e32 v230, v230, v231
	v_add_f32_e32 v230, v232, v230
	v_add_f32_e32 v230, v233, v230
	v_add_f32_e32 v14, v14, v230
	v_pk_add_f32 v[124:125], v[124:125], v[164:165]
	v_pk_add_f32 v[126:127], v[126:127], v[166:167]
	global_store_dwordx4 v59, v[124:127], s[10:11] offset:192
	v_pk_mul_f32 v[224:225], v[212:213], v[124:125]
	v_pk_mul_f32 v[226:227], v[214:215], v[126:127]
	v_cvt_pk_bf16_f32 v228, v224, v225
	v_cvt_pk_bf16_f32 v229, v226, v227
	global_store_dwordx2 v63, v[228:229], s[28:29] offset:96
	v_pk_mul_f32 v[230:231], v[124:125], v[124:125]
	v_pk_mul_f32 v[232:233], v[126:127], v[126:127]
	v_add_f32_e32 v230, v230, v231
	v_add_f32_e32 v230, v232, v230
	v_add_f32_e32 v15, v233, v230
	v_pk_add_f32 v[140:141], v[140:141], v[180:181]
	v_pk_add_f32 v[142:143], v[142:143], v[182:183]
	global_store_dwordx4 v59, v[140:143], s[10:11] offset:256
	v_pk_mul_f32 v[224:225], v[216:217], v[140:141]
	v_pk_mul_f32 v[226:227], v[218:219], v[142:143]
	v_cvt_pk_bf16_f32 v228, v224, v225
	v_cvt_pk_bf16_f32 v229, v226, v227
	global_store_dwordx2 v63, v[228:229], s[28:29] offset:128
	v_pk_mul_f32 v[230:231], v[140:141], v[140:141]
	v_pk_mul_f32 v[232:233], v[142:143], v[142:143]
	v_add_f32_e32 v230, v230, v231
	v_add_f32_e32 v230, v232, v230
	v_add_f32_e32 v230, v233, v230
	v_add_f32_e32 v15, v15, v230
	v_pk_add_f32 v[156:157], v[156:157], v[196:197]
	v_pk_add_f32 v[158:159], v[158:159], v[198:199]
	global_store_dwordx4 v59, v[156:159], s[10:11] offset:320
	v_pk_mul_f32 v[224:225], v[220:221], v[156:157]
	v_pk_mul_f32 v[226:227], v[222:223], v[158:159]
	v_cvt_pk_bf16_f32 v228, v224, v225
	v_cvt_pk_bf16_f32 v229, v226, v227
	global_store_dwordx2 v63, v[228:229], s[28:29] offset:160
	v_pk_mul_f32 v[230:231], v[156:157], v[156:157]
	v_pk_mul_f32 v[232:233], v[158:159], v[158:159]
	v_add_f32_e32 v230, v230, v231
	v_add_f32_e32 v230, v232, v230
	v_add_f32_e32 v230, v233, v230
	v_add_f32_e32 v15, v15, v230
	ds_bpermute_b32 v224, v13, v234
	ds_bpermute_b32 v225, v13, v235
	ds_bpermute_b32 v226, v13, v236
	ds_bpermute_b32 v227, v13, v237
	ds_bpermute_b32 v228, v13, v238
	ds_bpermute_b32 v229, v13, v239
	ds_bpermute_b32 v230, v13, v14
	ds_bpermute_b32 v231, v13, v15
	s_waitcnt lgkmcnt(0)
	v_add_f32_e32 v234, v234, v224
	v_add_f32_e32 v235, v235, v225
	v_add_f32_e32 v236, v236, v226
	v_add_f32_e32 v237, v237, v227
	v_add_f32_e32 v238, v238, v228
	v_add_f32_e32 v239, v239, v229
	v_add_f32_e32 v14, v14, v230
	v_add_f32_e32 v15, v15, v231
	ds_bpermute_b32 v224, v12, v234
	ds_bpermute_b32 v225, v12, v235
	ds_bpermute_b32 v226, v12, v236
	ds_bpermute_b32 v227, v12, v237
	ds_bpermute_b32 v228, v12, v238
	ds_bpermute_b32 v229, v12, v239
	ds_bpermute_b32 v230, v12, v14
	ds_bpermute_b32 v231, v12, v15
	s_waitcnt lgkmcnt(0)
	v_add_f32_e32 v234, v234, v224
	v_add_f32_e32 v235, v235, v225
	v_add_f32_e32 v236, v236, v226
	v_add_f32_e32 v237, v237, v227
	v_add_f32_e32 v238, v238, v228
	v_add_f32_e32 v239, v239, v229
	v_add_f32_e32 v14, v14, v230
	v_add_f32_e32 v15, v15, v231
	s_and_saveexec_b64 s[2:3], vcc
	global_store_dwordx2 v8, v[234:235], s[26:27]
	global_store_dwordx2 v9, v[236:237], s[26:27]
	global_store_dwordx2 v10, v[238:239], s[26:27]
	global_store_dwordx2 v11, v[14:15], s[26:27]
	s_or_b64 exec, exec, s[2:3]

	.amdhsa_kernel _Z7gemm128ILi1ELi96EEv8GemmArgs
		.amdhsa_group_segment_fixed_size 57344
		.amdhsa_private_segment_fixed_size 0
		.amdhsa_kernarg_size 80
		.amdhsa_user_sgpr_count 2
		.amdhsa_user_sgpr_dispatch_ptr 0
		.amdhsa_user_sgpr_queue_ptr 0
		.amdhsa_user_sgpr_kernarg_segment_ptr 1
		.amdhsa_user_sgpr_dispatch_id 0
		.amdhsa_user_sgpr_kernarg_preload_length 0
		.amdhsa_user_sgpr_kernarg_preload_offset 0
		.amdhsa_user_sgpr_private_segment_size 0
		.amdhsa_uses_dynamic_stack 0
		.amdhsa_enable_private_segment 0
		.amdhsa_system_sgpr_workgroup_id_x 1
		.amdhsa_system_sgpr_workgroup_id_y 0
		.amdhsa_system_sgpr_workgroup_id_z 0
		.amdhsa_system_sgpr_workgroup_info 0
		.amdhsa_system_vgpr_workitem_id 0
		.amdhsa_next_free_vgpr 256
		.amdhsa_next_free_sgpr 31
		.amdhsa_accum_offset 256
		.amdhsa_reserve_vcc 1
		.amdhsa_float_round_mode_32 0
		.amdhsa_float_round_mode_16_64 0
		.amdhsa_float_denorm_mode_32 3
		.amdhsa_float_denorm_mode_16_64 3
		.amdhsa_dx10_clamp 1
		.amdhsa_ieee_mode 1
		.amdhsa_fp16_overflow 0
		.amdhsa_tg_split 0
		.amdhsa_exception_fp_ieee_invalid_op 0
		.amdhsa_exception_fp_denorm_src 0
		.amdhsa_exception_fp_ieee_div_zero 0
		.amdhsa_exception_fp_ieee_overflow 0
		.amdhsa_exception_fp_ieee_underflow 0
		.amdhsa_exception_fp_ieee_inexact 0
		.amdhsa_exception_int_div_zero 0
	.end_amdhsa_kernel

amdhsa.kernels:
  - .agpr_count:     0
    .args:
      - .offset:         0
        .size:           136
        .value_kind:     by_value
      - .offset:         136
        .size:           4
        .value_kind:     hidden_block_count_x
      - .offset:         140
        .size:           4
        .value_kind:     hidden_block_count_y
      - .offset:         144
        .size:           4
        .value_kind:     hidden_block_count_z
      - .offset:         148
        .size:           2
        .value_kind:     hidden_group_size_x
      - .offset:         150
        .size:           2
        .value_kind:     hidden_group_size_y
      - .offset:         152
        .size:           2
        .value_kind:     hidden_group_size_z
      - .offset:         154
        .size:           2
        .value_kind:     hidden_remainder_x
      - .offset:         156
        .size:           2
        .value_kind:     hidden_remainder_y
      - .offset:         158
        .size:           2
        .value_kind:     hidden_remainder_z
      - .offset:         176
        .size:           8
        .value_kind:     hidden_global_offset_x
      - .offset:         184
        .size:           8
        .value_kind:     hidden_global_offset_y
      - .offset:         192
        .size:           8
        .value_kind:     hidden_global_offset_z
      - .offset:         200
        .size:           2
        .value_kind:     hidden_grid_dims
    .group_segment_fixed_size: 16640
    .kernarg_segment_align: 8
    .kernarg_segment_size: 392
    .language:       OpenCL C
    .language_version:
      - 2
      - 0
    .max_flat_workgroup_size: 256
    .name:           _Z11prep_kernel8PrepArgs
    .private_segment_fixed_size: 0
    .sgpr_count:     26
    .sgpr_spill_count: 0
    .symbol:         _Z11prep_kernel8PrepArgs.kd
    .uniform_work_group_size: 1
    .uses_dynamic_stack: false
    .vgpr_count:     46
    .vgpr_spill_count: 0
    .wavefront_size: 64
  - .agpr_count:     0
    .args:
      - .offset:         0
        .size:           216
        .value_kind:     by_value
    .group_segment_fixed_size: 0
    .kernarg_segment_align: 8
    .kernarg_segment_size: 216
    .language:       OpenCL C
    .language_version:
      - 2
      - 0
    .max_flat_workgroup_size: 512
    .name:           _Z11attn_kernel8AttnArgs
    .private_segment_fixed_size: 0
    .sgpr_count:     82
    .sgpr_spill_count: 0
    .symbol:         _Z11attn_kernel8AttnArgs.kd
    .uniform_work_group_size: 1
    .uses_dynamic_stack: false
    .vgpr_count:     220
    .vgpr_spill_count: 0
    .wavefront_size: 64
  - .agpr_count:     0
    .args:
      - .offset:         0
        .size:           80
        .value_kind:     by_value
    .group_segment_fixed_size: 57344
    .kernarg_segment_align: 8
    .kernarg_segment_size: 80
    .language:       OpenCL C
    .language_version:
      - 2
      - 0
    .max_flat_workgroup_size: 256
    .name:           _Z7gemm128ILi1ELi96EEv8GemmArgs
    .private_segment_fixed_size: 0
    .sgpr_count:     37
    .sgpr_spill_count: 0
    .symbol:         _Z7gemm128ILi1ELi96EEv8GemmArgs.kd
    .uniform_work_group_size: 1
    .uses_dynamic_stack: false
    .vgpr_count:     256
    .vgpr_spill_count: 0
    .wavefront_size: 64
  - .agpr_count:     0
    .args:
      - .offset:         0
        .size:           80
        .value_kind:     by_value
    .group_segment_fixed_size: 0
    .kernarg_segment_align: 8
    .kernarg_segment_size: 80
    .language:       OpenCL C
    .language_version:
      - 2
      - 0
    .max_flat_workgroup_size: 256
    .name:           _Z7gemm128ILi2ELi128EEv8GemmArgs
    .private_segment_fixed_size: 0
    .sgpr_count:     22
    .sgpr_spill_count: 0
    .symbol:         _Z7gemm128ILi2ELi128EEv8GemmArgs.kd
    .uniform_work_group_size: 1
    .uses_dynamic_stack: false
    .vgpr_count:     166
    .vgpr_spill_count: 0
    .wavefront_size: 64
  - .agpr_count:     0
    .args:
      - .offset:         0
        .size:           80
        .value_kind:     by_value
    .group_segment_fixed_size: 98304
    .kernarg_segment_align: 8
    .kernarg_segment_size: 80
    .language:       OpenCL C
    .language_version:
      - 2
      - 0
    .max_flat_workgroup_size: 256
    .name:           _Z7gemm128ILi3ELi96EEv8GemmArgs
    .private_segment_fixed_size: 0
    .sgpr_count:     30
    .sgpr_spill_count: 0
    .symbol:         _Z7gemm128ILi3ELi96EEv8GemmArgs.kd
    .uniform_work_group_size: 1
    .uses_dynamic_stack: false
    .vgpr_count:     256
    .vgpr_spill_count: 0
    .wavefront_size: 64
  - .agpr_count:     0
    .args:
      - .offset:         0
        .size:           32
        .value_kind:     by_value
      - .offset:         32
        .size:           56
        .value_kind:     by_value
    .group_segment_fixed_size: 0
    .kernarg_segment_align: 8
    .kernarg_segment_size: 88
    .language:       OpenCL C
    .language_version:
      - 2
      - 0
    .max_flat_workgroup_size: 512
    .name:           _Z8gemm_bigIN3pg86EpiQKVEEvNS0_4GemmET_
    .private_segment_fixed_size: 0
    .sgpr_count:     58
    .sgpr_spill_count: 0
    .symbol:         _Z8gemm_bigIN3pg86EpiQKVEEvNS0_4GemmET_.kd
    .uniform_work_group_size: 1
    .uses_dynamic_stack: false
    .vgpr_count:     228
    .vgpr_spill_count: 0
    .wavefront_size: 64
  - .agpr_count:     0
    .args:
      - .offset:         0
        .size:           32
        .value_kind:     by_value
      - .offset:         32
        .size:           32
        .value_kind:     by_value
    .group_segment_fixed_size: 0
    .kernarg_segment_align: 8
    .kernarg_segment_size: 64
    .language:       OpenCL C
    .language_version:
      - 2
      - 0
    .max_flat_workgroup_size: 512
    .name:           _Z8gemm_bigIN3pg85EpiUPEEvNS0_4GemmET_
    .private_segment_fixed_size: 0
    .sgpr_count:     50
    .sgpr_spill_count: 0
    .symbol:         _Z8gemm_bigIN3pg85EpiUPEEvNS0_4GemmET_.kd
    .uniform_work_group_size: 1
    .uses_dynamic_stack: false
    .vgpr_count:     226
    .vgpr_spill_count: 0
    .wavefront_size: 64
